# combo1 + hand-written P10 epilogue: rolling dwordx4 residual loads (permlane re-split), whole-cache-line f32 stores via DPP row_ror:8
# speedup vs baseline: 1.0136x; 1.0136x over previous
.LBB0_1361:
	s_andn2_b64 vcc, exec, s[0:1]
	s_mov_b64 s[0:1], -1
	s_ashr_i32 s17, s24, 4
	s_mul_hi_i32 s19, s17, 0x18000
	s_mul_i32 s17, s17, 0x18000
	s_add_u32 s26, s45, s17
	s_addc_u32 s27, s46, s19
	v_lshl_or_b32 v238, s54, 8, v223
	v_mov_b32_e32 v239, 0
	v_lshl_add_u64 v[240:241], v[238:239], 2, s[26:27]
	global_load_dwordx4 v[176:179], v[240:241], off
	global_load_dwordx4 v[180:183], v[240:241], off offset:64
	global_load_dwordx4 v[184:187], v[240:241], off offset:512
	global_load_dwordx4 v[188:191], v[240:241], off offset:576
	v_lshl_add_u32 v242, s24, 8, v206
	v_mov_b32_e32 v243, 0
	v_lshlrev_b64 v[192:193], 13, v[242:243]
	v_lshl_add_u64 v[192:193], v[192:193], 0, s[8:9]
	v_and_b32_e32 v244, 12, v223
	v_add_u32_e32 v244, v244, v238
	v_mov_b32_e32 v245, 0
	v_lshl_add_u64 v[192:193], v[244:245], 1, v[192:193]
	v_and_b32_e32 v242, -9, v206
	v_lshl_add_u32 v242, s24, 8, v242
	v_lshlrev_b64 v[194:195], 14, v[242:243]
	v_lshl_add_u64 v[194:195], v[194:195], 0, s[4:5]
	v_lshl_add_u64 v[194:195], v[238:239], 2, v[194:195]
	v_and_b32_e32 v244, 8, v206
	v_lshlrev_b32_e32 v244, 3, v244
	v_lshl_add_u64 v[194:195], v[244:245], 0, v[194:195]
	s_mov_b32 s26, 0x0
	s_mov_b32 s27, 0
	v_lshl_add_u64 v[196:197], v[192:193], 0, s[26:27]
	global_load_dwordx4 v[0:3], v[196:197], off
	s_mov_b32 s26, 0x0
	s_mov_b32 s27, 0
	v_lshl_add_u64 v[196:197], v[192:193], 0, s[26:27]
	global_load_dwordx4 v[4:7], v[196:197], off offset:256
	s_mov_b32 s26, 0x20000
	s_mov_b32 s27, 0
	v_lshl_add_u64 v[196:197], v[192:193], 0, s[26:27]
	global_load_dwordx4 v[8:11], v[196:197], off
	s_mov_b32 s26, 0x20000
	s_mov_b32 s27, 0
	v_lshl_add_u64 v[196:197], v[192:193], 0, s[26:27]
	global_load_dwordx4 v[12:15], v[196:197], off offset:256
	s_mov_b32 s26, 0x40000
	s_mov_b32 s27, 0
	v_lshl_add_u64 v[196:197], v[192:193], 0, s[26:27]
	global_load_dwordx4 v[16:19], v[196:197], off
	s_mov_b32 s26, 0x40000
	s_mov_b32 s27, 0
	v_lshl_add_u64 v[196:197], v[192:193], 0, s[26:27]
	global_load_dwordx4 v[20:23], v[196:197], off offset:256
	s_mov_b32 s26, 0x60000
	s_mov_b32 s27, 0
	v_lshl_add_u64 v[196:197], v[192:193], 0, s[26:27]
	global_load_dwordx4 v[24:27], v[196:197], off
	s_mov_b32 s26, 0x60000
	s_mov_b32 s27, 0
	v_lshl_add_u64 v[196:197], v[192:193], 0, s[26:27]
	global_load_dwordx4 v[28:31], v[196:197], off offset:256
	s_waitcnt vmcnt(8)
	v_mul_f32_e32 v176, s14, v176
	v_mul_f32_e32 v177, s14, v177
	v_mul_f32_e32 v178, s14, v178
	v_mul_f32_e32 v179, s14, v179
	v_mul_f32_e32 v180, s14, v180
	v_mul_f32_e32 v181, s14, v181
	v_mul_f32_e32 v182, s14, v182
	v_mul_f32_e32 v183, s14, v183
	v_mul_f32_e32 v184, s14, v184
	v_mul_f32_e32 v185, s14, v185
	v_mul_f32_e32 v186, s14, v186
	v_mul_f32_e32 v187, s14, v187
	v_mul_f32_e32 v188, s14, v188
	v_mul_f32_e32 v189, s14, v189
	v_mul_f32_e32 v190, s14, v190
	v_mul_f32_e32 v191, s14, v191
	s_waitcnt vmcnt(7)
	v_permlane16_swap_b32_e32 v0, v2
	v_permlane16_swap_b32_e32 v1, v3
	s_nop 1
	v_permlane32_swap_b32_e32 v0, v2
	v_permlane32_swap_b32_e32 v1, v3
	s_nop 1
	v_lshlrev_b32_e32 v226, 16, v0
	v_and_b32_e32 v227, 0xffff0000, v0
	v_lshlrev_b32_e32 v228, 16, v1
	v_and_b32_e32 v229, 0xffff0000, v1
	v_lshlrev_b32_e32 v230, 16, v2
	v_and_b32_e32 v231, 0xffff0000, v2
	v_lshlrev_b32_e32 v232, 16, v3
	v_and_b32_e32 v233, 0xffff0000, v3
	v_fma_f32 v226, v156, v176, v226
	v_fma_f32 v227, v157, v177, v227
	v_fma_f32 v228, v158, v178, v228
	v_fma_f32 v229, v159, v179, v229
	v_fma_f32 v230, v152, v180, v230
	v_fma_f32 v231, v153, v181, v231
	v_fma_f32 v232, v154, v182, v232
	v_fma_f32 v233, v155, v183, v233
	v_mov_b32_e32 v234, v230
	v_mov_b32_e32 v235, v231
	v_mov_b32_e32 v236, v232
	v_mov_b32_e32 v237, v233
	s_mov_b32 s26, 0x0
	s_mov_b32 s27, 0
	v_lshl_add_u64 v[198:199], v[194:195], 0, s[26:27]
	v_mov_b32_dpp v230, v226 row_ror:8 row_mask:0xf bank_mask:0x3
	v_mov_b32_dpp v231, v227 row_ror:8 row_mask:0xf bank_mask:0x3
	v_mov_b32_dpp v232, v228 row_ror:8 row_mask:0xf bank_mask:0x3
	v_mov_b32_dpp v233, v229 row_ror:8 row_mask:0xf bank_mask:0x3
	v_mov_b32_dpp v226, v234 row_ror:8 row_mask:0xf bank_mask:0xc
	v_mov_b32_dpp v227, v235 row_ror:8 row_mask:0xf bank_mask:0xc
	v_mov_b32_dpp v228, v236 row_ror:8 row_mask:0xf bank_mask:0xc
	v_mov_b32_dpp v229, v237 row_ror:8 row_mask:0xf bank_mask:0xc
	global_store_dwordx4 v[198:199], v[226:229], off
	s_mov_b32 s26, 0x20000
	s_mov_b32 s27, 0
	v_lshl_add_u64 v[198:199], v[198:199], 0, s[26:27]
	global_store_dwordx4 v[198:199], v[230:233], off
	s_nop 1
	s_mov_b32 s26, 0x100000
	s_mov_b32 s27, 0
	v_lshl_add_u64 v[196:197], v[192:193], 0, s[26:27]
	global_load_dwordx4 v[0:3], v[196:197], off
	s_waitcnt vmcnt(9)
	v_permlane16_swap_b32_e32 v4, v6
	v_permlane16_swap_b32_e32 v5, v7
	s_nop 1
	v_permlane32_swap_b32_e32 v4, v6
	v_permlane32_swap_b32_e32 v5, v7
	s_nop 1
	v_lshlrev_b32_e32 v226, 16, v4
	v_and_b32_e32 v227, 0xffff0000, v4
	v_lshlrev_b32_e32 v228, 16, v5
	v_and_b32_e32 v229, 0xffff0000, v5
	v_lshlrev_b32_e32 v230, 16, v6
	v_and_b32_e32 v231, 0xffff0000, v6
	v_lshlrev_b32_e32 v232, 16, v7
	v_and_b32_e32 v233, 0xffff0000, v7
	v_fma_f32 v226, v148, v184, v226
	v_fma_f32 v227, v149, v185, v227
	v_fma_f32 v228, v150, v186, v228
	v_fma_f32 v229, v151, v187, v229
	v_fma_f32 v230, v140, v188, v230
	v_fma_f32 v231, v141, v189, v231
	v_fma_f32 v232, v142, v190, v232
	v_fma_f32 v233, v143, v191, v233
	v_mov_b32_e32 v234, v230
	v_mov_b32_e32 v235, v231
	v_mov_b32_e32 v236, v232
	v_mov_b32_e32 v237, v233
	s_mov_b32 s26, 0x0
	s_mov_b32 s27, 0
	v_lshl_add_u64 v[198:199], v[194:195], 0, s[26:27]
	v_mov_b32_dpp v230, v226 row_ror:8 row_mask:0xf bank_mask:0x3
	v_mov_b32_dpp v231, v227 row_ror:8 row_mask:0xf bank_mask:0x3
	v_mov_b32_dpp v232, v228 row_ror:8 row_mask:0xf bank_mask:0x3
	v_mov_b32_dpp v233, v229 row_ror:8 row_mask:0xf bank_mask:0x3
	v_mov_b32_dpp v226, v234 row_ror:8 row_mask:0xf bank_mask:0xc
	v_mov_b32_dpp v227, v235 row_ror:8 row_mask:0xf bank_mask:0xc
	v_mov_b32_dpp v228, v236 row_ror:8 row_mask:0xf bank_mask:0xc
	v_mov_b32_dpp v229, v237 row_ror:8 row_mask:0xf bank_mask:0xc
	global_store_dwordx4 v[198:199], v[226:229], off offset:512
	s_mov_b32 s26, 0x20000
	s_mov_b32 s27, 0
	v_lshl_add_u64 v[198:199], v[198:199], 0, s[26:27]
	global_store_dwordx4 v[198:199], v[230:233], off offset:512
	s_nop 1
	s_mov_b32 s26, 0x100000
	s_mov_b32 s27, 0
	v_lshl_add_u64 v[196:197], v[192:193], 0, s[26:27]
	global_load_dwordx4 v[4:7], v[196:197], off offset:256
	s_waitcnt vmcnt(11)
	v_permlane16_swap_b32_e32 v8, v10
	v_permlane16_swap_b32_e32 v9, v11
	s_nop 1
	v_permlane32_swap_b32_e32 v8, v10
	v_permlane32_swap_b32_e32 v9, v11
	s_nop 1
	v_lshlrev_b32_e32 v226, 16, v8
	v_and_b32_e32 v227, 0xffff0000, v8
	v_lshlrev_b32_e32 v228, 16, v9
	v_and_b32_e32 v229, 0xffff0000, v9
	v_lshlrev_b32_e32 v230, 16, v10
	v_and_b32_e32 v231, 0xffff0000, v10
	v_lshlrev_b32_e32 v232, 16, v11
	v_and_b32_e32 v233, 0xffff0000, v11
	v_fma_f32 v226, v144, v176, v226
	v_fma_f32 v227, v145, v177, v227
	v_fma_f32 v228, v146, v178, v228
	v_fma_f32 v229, v147, v179, v229
	v_fma_f32 v230, v136, v180, v230
	v_fma_f32 v231, v137, v181, v231
	v_fma_f32 v232, v138, v182, v232
	v_fma_f32 v233, v139, v183, v233
	v_mov_b32_e32 v234, v230
	v_mov_b32_e32 v235, v231
	v_mov_b32_e32 v236, v232
	v_mov_b32_e32 v237, v233
	s_mov_b32 s26, 0x40000
	s_mov_b32 s27, 0
	v_lshl_add_u64 v[198:199], v[194:195], 0, s[26:27]
	v_mov_b32_dpp v230, v226 row_ror:8 row_mask:0xf bank_mask:0x3
	v_mov_b32_dpp v231, v227 row_ror:8 row_mask:0xf bank_mask:0x3
	v_mov_b32_dpp v232, v228 row_ror:8 row_mask:0xf bank_mask:0x3
	v_mov_b32_dpp v233, v229 row_ror:8 row_mask:0xf bank_mask:0x3
	v_mov_b32_dpp v226, v234 row_ror:8 row_mask:0xf bank_mask:0xc
	v_mov_b32_dpp v227, v235 row_ror:8 row_mask:0xf bank_mask:0xc
	v_mov_b32_dpp v228, v236 row_ror:8 row_mask:0xf bank_mask:0xc
	v_mov_b32_dpp v229, v237 row_ror:8 row_mask:0xf bank_mask:0xc
	global_store_dwordx4 v[198:199], v[226:229], off
	s_mov_b32 s26, 0x20000
	s_mov_b32 s27, 0
	v_lshl_add_u64 v[198:199], v[198:199], 0, s[26:27]
	global_store_dwordx4 v[198:199], v[230:233], off
	s_nop 1
	s_mov_b32 s26, 0x120000
	s_mov_b32 s27, 0
	v_lshl_add_u64 v[196:197], v[192:193], 0, s[26:27]
	global_load_dwordx4 v[8:11], v[196:197], off
	s_waitcnt vmcnt(13)
	v_permlane16_swap_b32_e32 v12, v14
	v_permlane16_swap_b32_e32 v13, v15
	s_nop 1
	v_permlane32_swap_b32_e32 v12, v14
	v_permlane32_swap_b32_e32 v13, v15
	s_nop 1
	v_lshlrev_b32_e32 v226, 16, v12
	v_and_b32_e32 v227, 0xffff0000, v12
	v_lshlrev_b32_e32 v228, 16, v13
	v_and_b32_e32 v229, 0xffff0000, v13
	v_lshlrev_b32_e32 v230, 16, v14
	v_and_b32_e32 v231, 0xffff0000, v14
	v_lshlrev_b32_e32 v232, 16, v15
	v_and_b32_e32 v233, 0xffff0000, v15
	v_fma_f32 v226, v132, v184, v226
	v_fma_f32 v227, v133, v185, v227
	v_fma_f32 v228, v134, v186, v228
	v_fma_f32 v229, v135, v187, v229
	v_fma_f32 v230, v128, v188, v230
	v_fma_f32 v231, v129, v189, v231
	v_fma_f32 v232, v130, v190, v232
	v_fma_f32 v233, v131, v191, v233
	v_mov_b32_e32 v234, v230
	v_mov_b32_e32 v235, v231
	v_mov_b32_e32 v236, v232
	v_mov_b32_e32 v237, v233
	s_mov_b32 s26, 0x40000
	s_mov_b32 s27, 0
	v_lshl_add_u64 v[198:199], v[194:195], 0, s[26:27]
	v_mov_b32_dpp v230, v226 row_ror:8 row_mask:0xf bank_mask:0x3
	v_mov_b32_dpp v231, v227 row_ror:8 row_mask:0xf bank_mask:0x3
	v_mov_b32_dpp v232, v228 row_ror:8 row_mask:0xf bank_mask:0x3
	v_mov_b32_dpp v233, v229 row_ror:8 row_mask:0xf bank_mask:0x3
	v_mov_b32_dpp v226, v234 row_ror:8 row_mask:0xf bank_mask:0xc
	v_mov_b32_dpp v227, v235 row_ror:8 row_mask:0xf bank_mask:0xc
	v_mov_b32_dpp v228, v236 row_ror:8 row_mask:0xf bank_mask:0xc
	v_mov_b32_dpp v229, v237 row_ror:8 row_mask:0xf bank_mask:0xc
	global_store_dwordx4 v[198:199], v[226:229], off offset:512
	s_mov_b32 s26, 0x20000
	s_mov_b32 s27, 0
	v_lshl_add_u64 v[198:199], v[198:199], 0, s[26:27]
	global_store_dwordx4 v[198:199], v[230:233], off offset:512
	s_nop 1
	s_mov_b32 s26, 0x120000
	s_mov_b32 s27, 0
	v_lshl_add_u64 v[196:197], v[192:193], 0, s[26:27]
	global_load_dwordx4 v[12:15], v[196:197], off offset:256
	s_waitcnt vmcnt(15)
	v_permlane16_swap_b32_e32 v16, v18
	v_permlane16_swap_b32_e32 v17, v19
	s_nop 1
	v_permlane32_swap_b32_e32 v16, v18
	v_permlane32_swap_b32_e32 v17, v19
	s_nop 1
	v_lshlrev_b32_e32 v226, 16, v16
	v_and_b32_e32 v227, 0xffff0000, v16
	v_lshlrev_b32_e32 v228, 16, v17
	v_and_b32_e32 v229, 0xffff0000, v17
	v_lshlrev_b32_e32 v230, 16, v18
	v_and_b32_e32 v231, 0xffff0000, v18
	v_lshlrev_b32_e32 v232, 16, v19
	v_and_b32_e32 v233, 0xffff0000, v19
	v_fma_f32 v226, v124, v176, v226
	v_fma_f32 v227, v125, v177, v227
	v_fma_f32 v228, v126, v178, v228
	v_fma_f32 v229, v127, v179, v229
	v_fma_f32 v230, v120, v180, v230
	v_fma_f32 v231, v121, v181, v231
	v_fma_f32 v232, v122, v182, v232
	v_fma_f32 v233, v123, v183, v233
	v_mov_b32_e32 v234, v230
	v_mov_b32_e32 v235, v231
	v_mov_b32_e32 v236, v232
	v_mov_b32_e32 v237, v233
	s_mov_b32 s26, 0x80000
	s_mov_b32 s27, 0
	v_lshl_add_u64 v[198:199], v[194:195], 0, s[26:27]
	v_mov_b32_dpp v230, v226 row_ror:8 row_mask:0xf bank_mask:0x3
	v_mov_b32_dpp v231, v227 row_ror:8 row_mask:0xf bank_mask:0x3
	v_mov_b32_dpp v232, v228 row_ror:8 row_mask:0xf bank_mask:0x3
	v_mov_b32_dpp v233, v229 row_ror:8 row_mask:0xf bank_mask:0x3
	v_mov_b32_dpp v226, v234 row_ror:8 row_mask:0xf bank_mask:0xc
	v_mov_b32_dpp v227, v235 row_ror:8 row_mask:0xf bank_mask:0xc
	v_mov_b32_dpp v228, v236 row_ror:8 row_mask:0xf bank_mask:0xc
	v_mov_b32_dpp v229, v237 row_ror:8 row_mask:0xf bank_mask:0xc
	global_store_dwordx4 v[198:199], v[226:229], off
	s_mov_b32 s26, 0x20000
	s_mov_b32 s27, 0
	v_lshl_add_u64 v[198:199], v[198:199], 0, s[26:27]
	global_store_dwordx4 v[198:199], v[230:233], off
	s_nop 1
	s_mov_b32 s26, 0x140000
	s_mov_b32 s27, 0
	v_lshl_add_u64 v[196:197], v[192:193], 0, s[26:27]
	global_load_dwordx4 v[16:19], v[196:197], off
	s_waitcnt vmcnt(17)
	v_permlane16_swap_b32_e32 v20, v22
	v_permlane16_swap_b32_e32 v21, v23
	s_nop 1
	v_permlane32_swap_b32_e32 v20, v22
	v_permlane32_swap_b32_e32 v21, v23
	s_nop 1
	v_lshlrev_b32_e32 v226, 16, v20
	v_and_b32_e32 v227, 0xffff0000, v20
	v_lshlrev_b32_e32 v228, 16, v21
	v_and_b32_e32 v229, 0xffff0000, v21
	v_lshlrev_b32_e32 v230, 16, v22
	v_and_b32_e32 v231, 0xffff0000, v22
	v_lshlrev_b32_e32 v232, 16, v23
	v_and_b32_e32 v233, 0xffff0000, v23
	v_fma_f32 v226, v116, v184, v226
	v_fma_f32 v227, v117, v185, v227
	v_fma_f32 v228, v118, v186, v228
	v_fma_f32 v229, v119, v187, v229
	v_fma_f32 v230, v108, v188, v230
	v_fma_f32 v231, v109, v189, v231
	v_fma_f32 v232, v110, v190, v232
	v_fma_f32 v233, v111, v191, v233
	v_mov_b32_e32 v234, v230
	v_mov_b32_e32 v235, v231
	v_mov_b32_e32 v236, v232
	v_mov_b32_e32 v237, v233
	s_mov_b32 s26, 0x80000
	s_mov_b32 s27, 0
	v_lshl_add_u64 v[198:199], v[194:195], 0, s[26:27]
	v_mov_b32_dpp v230, v226 row_ror:8 row_mask:0xf bank_mask:0x3
	v_mov_b32_dpp v231, v227 row_ror:8 row_mask:0xf bank_mask:0x3
	v_mov_b32_dpp v232, v228 row_ror:8 row_mask:0xf bank_mask:0x3
	v_mov_b32_dpp v233, v229 row_ror:8 row_mask:0xf bank_mask:0x3
	v_mov_b32_dpp v226, v234 row_ror:8 row_mask:0xf bank_mask:0xc
	v_mov_b32_dpp v227, v235 row_ror:8 row_mask:0xf bank_mask:0xc
	v_mov_b32_dpp v228, v236 row_ror:8 row_mask:0xf bank_mask:0xc
	v_mov_b32_dpp v229, v237 row_ror:8 row_mask:0xf bank_mask:0xc
	global_store_dwordx4 v[198:199], v[226:229], off offset:512
	s_mov_b32 s26, 0x20000
	s_mov_b32 s27, 0
	v_lshl_add_u64 v[198:199], v[198:199], 0, s[26:27]
	global_store_dwordx4 v[198:199], v[230:233], off offset:512
	s_nop 1
	s_mov_b32 s26, 0x140000
	s_mov_b32 s27, 0
	v_lshl_add_u64 v[196:197], v[192:193], 0, s[26:27]
	global_load_dwordx4 v[20:23], v[196:197], off offset:256
	s_waitcnt vmcnt(19)
	v_permlane16_swap_b32_e32 v24, v26
	v_permlane16_swap_b32_e32 v25, v27
	s_nop 1
	v_permlane32_swap_b32_e32 v24, v26
	v_permlane32_swap_b32_e32 v25, v27
	s_nop 1
	v_lshlrev_b32_e32 v226, 16, v24
	v_and_b32_e32 v227, 0xffff0000, v24
	v_lshlrev_b32_e32 v228, 16, v25
	v_and_b32_e32 v229, 0xffff0000, v25
	v_lshlrev_b32_e32 v230, 16, v26
	v_and_b32_e32 v231, 0xffff0000, v26
	v_lshlrev_b32_e32 v232, 16, v27
	v_and_b32_e32 v233, 0xffff0000, v27
	v_fma_f32 v226, v112, v176, v226
	v_fma_f32 v227, v113, v177, v227
	v_fma_f32 v228, v114, v178, v228
	v_fma_f32 v229, v115, v179, v229
	v_fma_f32 v230, v104, v180, v230
	v_fma_f32 v231, v105, v181, v231
	v_fma_f32 v232, v106, v182, v232
	v_fma_f32 v233, v107, v183, v233
	v_mov_b32_e32 v234, v230
	v_mov_b32_e32 v235, v231
	v_mov_b32_e32 v236, v232
	v_mov_b32_e32 v237, v233
	s_mov_b32 s26, 0xc0000
	s_mov_b32 s27, 0
	v_lshl_add_u64 v[198:199], v[194:195], 0, s[26:27]
	v_mov_b32_dpp v230, v226 row_ror:8 row_mask:0xf bank_mask:0x3
	v_mov_b32_dpp v231, v227 row_ror:8 row_mask:0xf bank_mask:0x3
	v_mov_b32_dpp v232, v228 row_ror:8 row_mask:0xf bank_mask:0x3
	v_mov_b32_dpp v233, v229 row_ror:8 row_mask:0xf bank_mask:0x3
	v_mov_b32_dpp v226, v234 row_ror:8 row_mask:0xf bank_mask:0xc
	v_mov_b32_dpp v227, v235 row_ror:8 row_mask:0xf bank_mask:0xc
	v_mov_b32_dpp v228, v236 row_ror:8 row_mask:0xf bank_mask:0xc
	v_mov_b32_dpp v229, v237 row_ror:8 row_mask:0xf bank_mask:0xc
	global_store_dwordx4 v[198:199], v[226:229], off
	s_mov_b32 s26, 0x20000
	s_mov_b32 s27, 0
	v_lshl_add_u64 v[198:199], v[198:199], 0, s[26:27]
	global_store_dwordx4 v[198:199], v[230:233], off
	s_nop 1
	s_mov_b32 s26, 0x160000
	s_mov_b32 s27, 0
	v_lshl_add_u64 v[196:197], v[192:193], 0, s[26:27]
	global_load_dwordx4 v[24:27], v[196:197], off
	s_waitcnt vmcnt(21)
	v_permlane16_swap_b32_e32 v28, v30
	v_permlane16_swap_b32_e32 v29, v31
	s_nop 1
	v_permlane32_swap_b32_e32 v28, v30
	v_permlane32_swap_b32_e32 v29, v31
	s_nop 1
	v_lshlrev_b32_e32 v226, 16, v28
	v_and_b32_e32 v227, 0xffff0000, v28
	v_lshlrev_b32_e32 v228, 16, v29
	v_and_b32_e32 v229, 0xffff0000, v29
	v_lshlrev_b32_e32 v230, 16, v30
	v_and_b32_e32 v231, 0xffff0000, v30
	v_lshlrev_b32_e32 v232, 16, v31
	v_and_b32_e32 v233, 0xffff0000, v31
	v_fma_f32 v226, v100, v184, v226
	v_fma_f32 v227, v101, v185, v227
	v_fma_f32 v228, v102, v186, v228
	v_fma_f32 v229, v103, v187, v229
	v_fma_f32 v230, v96, v188, v230
	v_fma_f32 v231, v97, v189, v231
	v_fma_f32 v232, v98, v190, v232
	v_fma_f32 v233, v99, v191, v233
	v_mov_b32_e32 v234, v230
	v_mov_b32_e32 v235, v231
	v_mov_b32_e32 v236, v232
	v_mov_b32_e32 v237, v233
	s_mov_b32 s26, 0xc0000
	s_mov_b32 s27, 0
	v_lshl_add_u64 v[198:199], v[194:195], 0, s[26:27]
	v_mov_b32_dpp v230, v226 row_ror:8 row_mask:0xf bank_mask:0x3
	v_mov_b32_dpp v231, v227 row_ror:8 row_mask:0xf bank_mask:0x3
	v_mov_b32_dpp v232, v228 row_ror:8 row_mask:0xf bank_mask:0x3
	v_mov_b32_dpp v233, v229 row_ror:8 row_mask:0xf bank_mask:0x3
	v_mov_b32_dpp v226, v234 row_ror:8 row_mask:0xf bank_mask:0xc
	v_mov_b32_dpp v227, v235 row_ror:8 row_mask:0xf bank_mask:0xc
	v_mov_b32_dpp v228, v236 row_ror:8 row_mask:0xf bank_mask:0xc
	v_mov_b32_dpp v229, v237 row_ror:8 row_mask:0xf bank_mask:0xc
	global_store_dwordx4 v[198:199], v[226:229], off offset:512
	s_mov_b32 s26, 0x20000
	s_mov_b32 s27, 0
	v_lshl_add_u64 v[198:199], v[198:199], 0, s[26:27]
	global_store_dwordx4 v[198:199], v[230:233], off offset:512
	s_nop 1
	s_mov_b32 s26, 0x160000
	s_mov_b32 s27, 0
	v_lshl_add_u64 v[196:197], v[192:193], 0, s[26:27]
	global_load_dwordx4 v[28:31], v[196:197], off offset:256
	s_waitcnt vmcnt(21)
	v_permlane16_swap_b32_e32 v0, v2
	v_permlane16_swap_b32_e32 v1, v3
	s_nop 1
	v_permlane32_swap_b32_e32 v0, v2
	v_permlane32_swap_b32_e32 v1, v3
	s_nop 1
	v_lshlrev_b32_e32 v226, 16, v0
	v_and_b32_e32 v227, 0xffff0000, v0
	v_lshlrev_b32_e32 v228, 16, v1
	v_and_b32_e32 v229, 0xffff0000, v1
	v_lshlrev_b32_e32 v230, 16, v2
	v_and_b32_e32 v231, 0xffff0000, v2
	v_lshlrev_b32_e32 v232, 16, v3
	v_and_b32_e32 v233, 0xffff0000, v3
	v_fma_f32 v226, v92, v176, v226
	v_fma_f32 v227, v93, v177, v227
	v_fma_f32 v228, v94, v178, v228
	v_fma_f32 v229, v95, v179, v229
	v_fma_f32 v230, v88, v180, v230
	v_fma_f32 v231, v89, v181, v231
	v_fma_f32 v232, v90, v182, v232
	v_fma_f32 v233, v91, v183, v233
	v_mov_b32_e32 v234, v230
	v_mov_b32_e32 v235, v231
	v_mov_b32_e32 v236, v232
	v_mov_b32_e32 v237, v233
	s_mov_b32 s26, 0x200000
	s_mov_b32 s27, 0
	v_lshl_add_u64 v[198:199], v[194:195], 0, s[26:27]
	v_mov_b32_dpp v230, v226 row_ror:8 row_mask:0xf bank_mask:0x3
	v_mov_b32_dpp v231, v227 row_ror:8 row_mask:0xf bank_mask:0x3
	v_mov_b32_dpp v232, v228 row_ror:8 row_mask:0xf bank_mask:0x3
	v_mov_b32_dpp v233, v229 row_ror:8 row_mask:0xf bank_mask:0x3
	v_mov_b32_dpp v226, v234 row_ror:8 row_mask:0xf bank_mask:0xc
	v_mov_b32_dpp v227, v235 row_ror:8 row_mask:0xf bank_mask:0xc
	v_mov_b32_dpp v228, v236 row_ror:8 row_mask:0xf bank_mask:0xc
	v_mov_b32_dpp v229, v237 row_ror:8 row_mask:0xf bank_mask:0xc
	global_store_dwordx4 v[198:199], v[226:229], off
	s_mov_b32 s26, 0x20000
	s_mov_b32 s27, 0
	v_lshl_add_u64 v[198:199], v[198:199], 0, s[26:27]
	global_store_dwordx4 v[198:199], v[230:233], off
	s_nop 1
	s_waitcnt vmcnt(20)
	v_permlane16_swap_b32_e32 v4, v6
	v_permlane16_swap_b32_e32 v5, v7
	s_nop 1
	v_permlane32_swap_b32_e32 v4, v6
	v_permlane32_swap_b32_e32 v5, v7
	s_nop 1
	v_lshlrev_b32_e32 v226, 16, v4
	v_and_b32_e32 v227, 0xffff0000, v4
	v_lshlrev_b32_e32 v228, 16, v5
	v_and_b32_e32 v229, 0xffff0000, v5
	v_lshlrev_b32_e32 v230, 16, v6
	v_and_b32_e32 v231, 0xffff0000, v6
	v_lshlrev_b32_e32 v232, 16, v7
	v_and_b32_e32 v233, 0xffff0000, v7
	v_fma_f32 v226, v84, v184, v226
	v_fma_f32 v227, v85, v185, v227
	v_fma_f32 v228, v86, v186, v228
	v_fma_f32 v229, v87, v187, v229
	v_fma_f32 v230, v76, v188, v230
	v_fma_f32 v231, v77, v189, v231
	v_fma_f32 v232, v78, v190, v232
	v_fma_f32 v233, v79, v191, v233
	v_mov_b32_e32 v234, v230
	v_mov_b32_e32 v235, v231
	v_mov_b32_e32 v236, v232
	v_mov_b32_e32 v237, v233
	s_mov_b32 s26, 0x200000
	s_mov_b32 s27, 0
	v_lshl_add_u64 v[198:199], v[194:195], 0, s[26:27]
	v_mov_b32_dpp v230, v226 row_ror:8 row_mask:0xf bank_mask:0x3
	v_mov_b32_dpp v231, v227 row_ror:8 row_mask:0xf bank_mask:0x3
	v_mov_b32_dpp v232, v228 row_ror:8 row_mask:0xf bank_mask:0x3
	v_mov_b32_dpp v233, v229 row_ror:8 row_mask:0xf bank_mask:0x3
	v_mov_b32_dpp v226, v234 row_ror:8 row_mask:0xf bank_mask:0xc
	v_mov_b32_dpp v227, v235 row_ror:8 row_mask:0xf bank_mask:0xc
	v_mov_b32_dpp v228, v236 row_ror:8 row_mask:0xf bank_mask:0xc
	v_mov_b32_dpp v229, v237 row_ror:8 row_mask:0xf bank_mask:0xc
	global_store_dwordx4 v[198:199], v[226:229], off offset:512
	s_mov_b32 s26, 0x20000
	s_mov_b32 s27, 0
	v_lshl_add_u64 v[198:199], v[198:199], 0, s[26:27]
	global_store_dwordx4 v[198:199], v[230:233], off offset:512
	s_nop 1
	s_waitcnt vmcnt(19)
	v_permlane16_swap_b32_e32 v8, v10
	v_permlane16_swap_b32_e32 v9, v11
	s_nop 1
	v_permlane32_swap_b32_e32 v8, v10
	v_permlane32_swap_b32_e32 v9, v11
	s_nop 1
	v_lshlrev_b32_e32 v226, 16, v8
	v_and_b32_e32 v227, 0xffff0000, v8
	v_lshlrev_b32_e32 v228, 16, v9
	v_and_b32_e32 v229, 0xffff0000, v9
	v_lshlrev_b32_e32 v230, 16, v10
	v_and_b32_e32 v231, 0xffff0000, v10
	v_lshlrev_b32_e32 v232, 16, v11
	v_and_b32_e32 v233, 0xffff0000, v11
	v_fma_f32 v226, v80, v176, v226
	v_fma_f32 v227, v81, v177, v227
	v_fma_f32 v228, v82, v178, v228
	v_fma_f32 v229, v83, v179, v229
	v_fma_f32 v230, v72, v180, v230
	v_fma_f32 v231, v73, v181, v231
	v_fma_f32 v232, v74, v182, v232
	v_fma_f32 v233, v75, v183, v233
	v_mov_b32_e32 v234, v230
	v_mov_b32_e32 v235, v231
	v_mov_b32_e32 v236, v232
	v_mov_b32_e32 v237, v233
	s_mov_b32 s26, 0x240000
	s_mov_b32 s27, 0
	v_lshl_add_u64 v[198:199], v[194:195], 0, s[26:27]
	v_mov_b32_dpp v230, v226 row_ror:8 row_mask:0xf bank_mask:0x3
	v_mov_b32_dpp v231, v227 row_ror:8 row_mask:0xf bank_mask:0x3
	v_mov_b32_dpp v232, v228 row_ror:8 row_mask:0xf bank_mask:0x3
	v_mov_b32_dpp v233, v229 row_ror:8 row_mask:0xf bank_mask:0x3
	v_mov_b32_dpp v226, v234 row_ror:8 row_mask:0xf bank_mask:0xc
	v_mov_b32_dpp v227, v235 row_ror:8 row_mask:0xf bank_mask:0xc
	v_mov_b32_dpp v228, v236 row_ror:8 row_mask:0xf bank_mask:0xc
	v_mov_b32_dpp v229, v237 row_ror:8 row_mask:0xf bank_mask:0xc
	global_store_dwordx4 v[198:199], v[226:229], off
	s_mov_b32 s26, 0x20000
	s_mov_b32 s27, 0
	v_lshl_add_u64 v[198:199], v[198:199], 0, s[26:27]
	global_store_dwordx4 v[198:199], v[230:233], off
	s_nop 1
	s_waitcnt vmcnt(18)
	v_permlane16_swap_b32_e32 v12, v14
	v_permlane16_swap_b32_e32 v13, v15
	s_nop 1
	v_permlane32_swap_b32_e32 v12, v14
	v_permlane32_swap_b32_e32 v13, v15
	s_nop 1
	v_lshlrev_b32_e32 v226, 16, v12
	v_and_b32_e32 v227, 0xffff0000, v12
	v_lshlrev_b32_e32 v228, 16, v13
	v_and_b32_e32 v229, 0xffff0000, v13
	v_lshlrev_b32_e32 v230, 16, v14
	v_and_b32_e32 v231, 0xffff0000, v14
	v_lshlrev_b32_e32 v232, 16, v15
	v_and_b32_e32 v233, 0xffff0000, v15
	v_fma_f32 v226, v68, v184, v226
	v_fma_f32 v227, v69, v185, v227
	v_fma_f32 v228, v70, v186, v228
	v_fma_f32 v229, v71, v187, v229
	v_fma_f32 v230, v60, v188, v230
	v_fma_f32 v231, v61, v189, v231
	v_fma_f32 v232, v62, v190, v232
	v_fma_f32 v233, v63, v191, v233
	v_mov_b32_e32 v234, v230
	v_mov_b32_e32 v235, v231
	v_mov_b32_e32 v236, v232
	v_mov_b32_e32 v237, v233
	s_mov_b32 s26, 0x240000
	s_mov_b32 s27, 0
	v_lshl_add_u64 v[198:199], v[194:195], 0, s[26:27]
	v_mov_b32_dpp v230, v226 row_ror:8 row_mask:0xf bank_mask:0x3
	v_mov_b32_dpp v231, v227 row_ror:8 row_mask:0xf bank_mask:0x3
	v_mov_b32_dpp v232, v228 row_ror:8 row_mask:0xf bank_mask:0x3
	v_mov_b32_dpp v233, v229 row_ror:8 row_mask:0xf bank_mask:0x3
	v_mov_b32_dpp v226, v234 row_ror:8 row_mask:0xf bank_mask:0xc
	v_mov_b32_dpp v227, v235 row_ror:8 row_mask:0xf bank_mask:0xc
	v_mov_b32_dpp v228, v236 row_ror:8 row_mask:0xf bank_mask:0xc
	v_mov_b32_dpp v229, v237 row_ror:8 row_mask:0xf bank_mask:0xc
	global_store_dwordx4 v[198:199], v[226:229], off offset:512
	s_mov_b32 s26, 0x20000
	s_mov_b32 s27, 0
	v_lshl_add_u64 v[198:199], v[198:199], 0, s[26:27]
	global_store_dwordx4 v[198:199], v[230:233], off offset:512
	s_nop 1
	s_waitcnt vmcnt(17)
	v_permlane16_swap_b32_e32 v16, v18
	v_permlane16_swap_b32_e32 v17, v19
	s_nop 1
	v_permlane32_swap_b32_e32 v16, v18
	v_permlane32_swap_b32_e32 v17, v19
	s_nop 1
	v_lshlrev_b32_e32 v226, 16, v16
	v_and_b32_e32 v227, 0xffff0000, v16
	v_lshlrev_b32_e32 v228, 16, v17
	v_and_b32_e32 v229, 0xffff0000, v17
	v_lshlrev_b32_e32 v230, 16, v18
	v_and_b32_e32 v231, 0xffff0000, v18
	v_lshlrev_b32_e32 v232, 16, v19
	v_and_b32_e32 v233, 0xffff0000, v19
	v_fma_f32 v226, v64, v176, v226
	v_fma_f32 v227, v65, v177, v227
	v_fma_f32 v228, v66, v178, v228
	v_fma_f32 v229, v67, v179, v229
	v_fma_f32 v230, v56, v180, v230
	v_fma_f32 v231, v57, v181, v231
	v_fma_f32 v232, v58, v182, v232
	v_fma_f32 v233, v59, v183, v233
	v_mov_b32_e32 v234, v230
	v_mov_b32_e32 v235, v231
	v_mov_b32_e32 v236, v232
	v_mov_b32_e32 v237, v233
	s_mov_b32 s26, 0x280000
	s_mov_b32 s27, 0
	v_lshl_add_u64 v[198:199], v[194:195], 0, s[26:27]
	v_mov_b32_dpp v230, v226 row_ror:8 row_mask:0xf bank_mask:0x3
	v_mov_b32_dpp v231, v227 row_ror:8 row_mask:0xf bank_mask:0x3
	v_mov_b32_dpp v232, v228 row_ror:8 row_mask:0xf bank_mask:0x3
	v_mov_b32_dpp v233, v229 row_ror:8 row_mask:0xf bank_mask:0x3
	v_mov_b32_dpp v226, v234 row_ror:8 row_mask:0xf bank_mask:0xc
	v_mov_b32_dpp v227, v235 row_ror:8 row_mask:0xf bank_mask:0xc
	v_mov_b32_dpp v228, v236 row_ror:8 row_mask:0xf bank_mask:0xc
	v_mov_b32_dpp v229, v237 row_ror:8 row_mask:0xf bank_mask:0xc
	global_store_dwordx4 v[198:199], v[226:229], off
	s_mov_b32 s26, 0x20000
	s_mov_b32 s27, 0
	v_lshl_add_u64 v[198:199], v[198:199], 0, s[26:27]
	global_store_dwordx4 v[198:199], v[230:233], off
	s_nop 1
	s_waitcnt vmcnt(16)
	v_permlane16_swap_b32_e32 v20, v22
	v_permlane16_swap_b32_e32 v21, v23
	s_nop 1
	v_permlane32_swap_b32_e32 v20, v22
	v_permlane32_swap_b32_e32 v21, v23
	s_nop 1
	v_lshlrev_b32_e32 v226, 16, v20
	v_and_b32_e32 v227, 0xffff0000, v20
	v_lshlrev_b32_e32 v228, 16, v21
	v_and_b32_e32 v229, 0xffff0000, v21
	v_lshlrev_b32_e32 v230, 16, v22
	v_and_b32_e32 v231, 0xffff0000, v22
	v_lshlrev_b32_e32 v232, 16, v23
	v_and_b32_e32 v233, 0xffff0000, v23
	v_fma_f32 v226, v52, v184, v226
	v_fma_f32 v227, v53, v185, v227
	v_fma_f32 v228, v54, v186, v228
	v_fma_f32 v229, v55, v187, v229
	v_fma_f32 v230, v44, v188, v230
	v_fma_f32 v231, v45, v189, v231
	v_fma_f32 v232, v46, v190, v232
	v_fma_f32 v233, v47, v191, v233
	v_mov_b32_e32 v234, v230
	v_mov_b32_e32 v235, v231
	v_mov_b32_e32 v236, v232
	v_mov_b32_e32 v237, v233
	s_mov_b32 s26, 0x280000
	s_mov_b32 s27, 0
	v_lshl_add_u64 v[198:199], v[194:195], 0, s[26:27]
	v_mov_b32_dpp v230, v226 row_ror:8 row_mask:0xf bank_mask:0x3
	v_mov_b32_dpp v231, v227 row_ror:8 row_mask:0xf bank_mask:0x3
	v_mov_b32_dpp v232, v228 row_ror:8 row_mask:0xf bank_mask:0x3
	v_mov_b32_dpp v233, v229 row_ror:8 row_mask:0xf bank_mask:0x3
	v_mov_b32_dpp v226, v234 row_ror:8 row_mask:0xf bank_mask:0xc
	v_mov_b32_dpp v227, v235 row_ror:8 row_mask:0xf bank_mask:0xc
	v_mov_b32_dpp v228, v236 row_ror:8 row_mask:0xf bank_mask:0xc
	v_mov_b32_dpp v229, v237 row_ror:8 row_mask:0xf bank_mask:0xc
	global_store_dwordx4 v[198:199], v[226:229], off offset:512
	s_mov_b32 s26, 0x20000
	s_mov_b32 s27, 0
	v_lshl_add_u64 v[198:199], v[198:199], 0, s[26:27]
	global_store_dwordx4 v[198:199], v[230:233], off offset:512
	s_nop 1
	s_waitcnt vmcnt(15)
	v_permlane16_swap_b32_e32 v24, v26
	v_permlane16_swap_b32_e32 v25, v27
	s_nop 1
	v_permlane32_swap_b32_e32 v24, v26
	v_permlane32_swap_b32_e32 v25, v27
	s_nop 1
	v_lshlrev_b32_e32 v226, 16, v24
	v_and_b32_e32 v227, 0xffff0000, v24
	v_lshlrev_b32_e32 v228, 16, v25
	v_and_b32_e32 v229, 0xffff0000, v25
	v_lshlrev_b32_e32 v230, 16, v26
	v_and_b32_e32 v231, 0xffff0000, v26
	v_lshlrev_b32_e32 v232, 16, v27
	v_and_b32_e32 v233, 0xffff0000, v27
	v_fma_f32 v226, v48, v176, v226
	v_fma_f32 v227, v49, v177, v227
	v_fma_f32 v228, v50, v178, v228
	v_fma_f32 v229, v51, v179, v229
	v_fma_f32 v230, v40, v180, v230
	v_fma_f32 v231, v41, v181, v231
	v_fma_f32 v232, v42, v182, v232
	v_fma_f32 v233, v43, v183, v233
	v_mov_b32_e32 v234, v230
	v_mov_b32_e32 v235, v231
	v_mov_b32_e32 v236, v232
	v_mov_b32_e32 v237, v233
	s_mov_b32 s26, 0x2c0000
	s_mov_b32 s27, 0
	v_lshl_add_u64 v[198:199], v[194:195], 0, s[26:27]
	v_mov_b32_dpp v230, v226 row_ror:8 row_mask:0xf bank_mask:0x3
	v_mov_b32_dpp v231, v227 row_ror:8 row_mask:0xf bank_mask:0x3
	v_mov_b32_dpp v232, v228 row_ror:8 row_mask:0xf bank_mask:0x3
	v_mov_b32_dpp v233, v229 row_ror:8 row_mask:0xf bank_mask:0x3
	v_mov_b32_dpp v226, v234 row_ror:8 row_mask:0xf bank_mask:0xc
	v_mov_b32_dpp v227, v235 row_ror:8 row_mask:0xf bank_mask:0xc
	v_mov_b32_dpp v228, v236 row_ror:8 row_mask:0xf bank_mask:0xc
	v_mov_b32_dpp v229, v237 row_ror:8 row_mask:0xf bank_mask:0xc
	global_store_dwordx4 v[198:199], v[226:229], off
	s_mov_b32 s26, 0x20000
	s_mov_b32 s27, 0
	v_lshl_add_u64 v[198:199], v[198:199], 0, s[26:27]
	global_store_dwordx4 v[198:199], v[230:233], off
	s_nop 1
	s_waitcnt vmcnt(14)
	v_permlane16_swap_b32_e32 v28, v30
	v_permlane16_swap_b32_e32 v29, v31
	s_nop 1
	v_permlane32_swap_b32_e32 v28, v30
	v_permlane32_swap_b32_e32 v29, v31
	s_nop 1
	v_lshlrev_b32_e32 v226, 16, v28
	v_and_b32_e32 v227, 0xffff0000, v28
	v_lshlrev_b32_e32 v228, 16, v29
	v_and_b32_e32 v229, 0xffff0000, v29
	v_lshlrev_b32_e32 v230, 16, v30
	v_and_b32_e32 v231, 0xffff0000, v30
	v_lshlrev_b32_e32 v232, 16, v31
	v_and_b32_e32 v233, 0xffff0000, v31
	v_fma_f32 v226, v36, v184, v226
	v_fma_f32 v227, v37, v185, v227
	v_fma_f32 v228, v38, v186, v228
	v_fma_f32 v229, v39, v187, v229
	v_fma_f32 v230, v32, v188, v230
	v_fma_f32 v231, v33, v189, v231
	v_fma_f32 v232, v34, v190, v232
	v_fma_f32 v233, v35, v191, v233
	v_mov_b32_e32 v234, v230
	v_mov_b32_e32 v235, v231
	v_mov_b32_e32 v236, v232
	v_mov_b32_e32 v237, v233
	s_mov_b32 s26, 0x2c0000
	s_mov_b32 s27, 0
	v_lshl_add_u64 v[198:199], v[194:195], 0, s[26:27]
	v_mov_b32_dpp v230, v226 row_ror:8 row_mask:0xf bank_mask:0x3
	v_mov_b32_dpp v231, v227 row_ror:8 row_mask:0xf bank_mask:0x3
	v_mov_b32_dpp v232, v228 row_ror:8 row_mask:0xf bank_mask:0x3
	v_mov_b32_dpp v233, v229 row_ror:8 row_mask:0xf bank_mask:0x3
	v_mov_b32_dpp v226, v234 row_ror:8 row_mask:0xf bank_mask:0xc
	v_mov_b32_dpp v227, v235 row_ror:8 row_mask:0xf bank_mask:0xc
	v_mov_b32_dpp v228, v236 row_ror:8 row_mask:0xf bank_mask:0xc
	v_mov_b32_dpp v229, v237 row_ror:8 row_mask:0xf bank_mask:0xc
	global_store_dwordx4 v[198:199], v[226:229], off offset:512
	s_mov_b32 s26, 0x20000
	s_mov_b32 s27, 0
	v_lshl_add_u64 v[198:199], v[198:199], 0, s[26:27]
	global_store_dwordx4 v[198:199], v[230:233], off offset:512
	s_nop 1
	s_cbranch_vccnz .LBB0_1350
	s_andn2_b64 vcc, exec, s[6:7]
	s_cbranch_vccnz .LBB0_1349
	s_barrier
	s_branch .LBB0_1349
